# stack14 = stack11 + expert-phase class lookup by one parallel compare (was a 7-step binary search over LDS) + router top-2: partial-logit reads of experts 3..7 issued together behind those of expert 2
# speedup vs baseline: 1.0040x; 1.0040x over previous
; DEVINL void phase4(const Params& P, unsigned char* smem) {
;     ...
;             const float g0 = LG(0), g1 = LG(1), g2 = LG(2), g3 = LG(3);
;             int gtop = 0; float gm = g0;
;             if (g1 > gm) { gm = g1; gtop = 1; } if (g2 > gm) { gm = g2; gtop = 2; } if (g3 > gm) { gm = g3; gtop = 3; }
;             const float gwt = 1.f / (expf(g0 - gm) + expf(g1 - gm) + expf(g2 - gm) + expf(g3 - gm));
;             int i1 = 0, i2 = 0; float v1 = -3.0e38f, v2 = -3.0e38f;
;             for (int e = 0; e < 8; ++e) {
;                 const float v = LG(4 + gtop * 8 + e);
;                 if (v > v1) { v2 = v1; i2 = i1; v1 = v; i1 = e; } else if (v > v2) { v2 = v; i2 = e; }
.LBB0_609:
	s_or_b64 exec, exec, s[10:11]
	v_add_u32_e32 v14, 0x12600, v9
	ds_read2st64_b32 v[16:17], v9 offset0:54 offset1:102
	ds_read2st64_b32 v[18:19], v9 offset0:150 offset1:198
	v_add_u32_e32 v21, 0x15600, v9
	ds_read_b32 v20, v8 offset:1536
	ds_read_b32 v23, v9 offset:62976
	ds_read_b32 v25, v14
	ds_read_b32 v14, v21
	ds_read2st64_b32 v[40:41], v9 offset0:55 offset1:103
	ds_read2st64_b32 v[42:43], v9 offset0:151 offset1:199
	ds_read_b32 v44, v8 offset:1792
	ds_read_b32 v45, v9 offset:63232
	v_add_u32_e32 v47, 0x12700, v9
	ds_read_b32 v46, v47
	v_add_u32_e32 v49, 0x15700, v9
	ds_read_b32 v48, v49
	ds_read2st64_b32 v[50:51], v9 offset0:56 offset1:104
	ds_read2st64_b32 v[52:53], v9 offset0:152 offset1:200
	ds_read_b32 v54, v8 offset:2048
	ds_read_b32 v55, v9 offset:63488
	v_add_u32_e32 v57, 0x12800, v9
	ds_read_b32 v56, v57
	v_add_u32_e32 v59, 0x15800, v9
	ds_read_b32 v58, v59
	ds_read2st64_b32 v[60:61], v9 offset0:57 offset1:105
	ds_read2st64_b32 v[62:63], v9 offset0:153 offset1:201
	ds_read_b32 v64, v8 offset:2304
	ds_read_b32 v65, v9 offset:63744
	v_add_u32_e32 v67, 0x12900, v9
	ds_read_b32 v66, v67
	v_add_u32_e32 v69, 0x15900, v9
	ds_read_b32 v68, v69
	ds_read2st64_b32 v[70:71], v9 offset0:58 offset1:106
	ds_read2st64_b32 v[72:73], v9 offset0:154 offset1:202
	ds_read_b32 v74, v8 offset:2560
	ds_read_b32 v75, v9 offset:64000
	v_add_u32_e32 v77, 0x12a00, v9
	ds_read_b32 v76, v77
	v_add_u32_e32 v79, 0x15a00, v9
	ds_read_b32 v78, v79
	ds_read2st64_b32 v[80:81], v9 offset0:59 offset1:107
	ds_read2st64_b32 v[82:83], v9 offset0:155 offset1:203
	ds_read_b32 v84, v8 offset:2816
	ds_read_b32 v85, v9 offset:64256
	v_add_u32_e32 v87, 0x12b00, v9
	ds_read_b32 v86, v87
	v_add_u32_e32 v89, 0x15b00, v9
	ds_read_b32 v88, v89
	v_mov_b32_e32 v10, 2
	s_waitcnt lgkmcnt(5)
	v_mov_b32_e32 v22, v16
	s_waitcnt lgkmcnt(4)
	v_mov_b32_e32 v21, v19
	v_mov_b32_e32 v24, v17
	s_waitcnt lgkmcnt(0)
	v_mov_b32_e32 v19, v14
	v_pk_add_f32 v[20:21], v[20:21], v[22:23]
	v_pk_add_f32 v[16:17], v[24:25], v[18:19]
	s_nop 0
	v_pk_add_f32 v[16:17], v[20:21], v[16:17]
	s_nop 0
	v_add_f32_e32 v14, v16, v17
	v_cmp_ngt_f32_e64 s[8:9], v14, v12
	s_and_saveexec_b64 s[10:11], s[8:9]
	s_cbranch_execz .LBB0_613
	v_cmp_gt_f32_e64 s[8:9], v14, v13
	s_and_saveexec_b64 s[12:13], s[8:9]
	v_mov_b32_e32 v15, 2
	v_mov_b32_e32 v13, v14
	s_or_b64 exec, exec, s[12:13]
	v_mov_b32_e32 v10, v11
	v_mov_b32_e32 v11, v15
	v_mov_b32_e32 v14, v12
	v_mov_b32_e32 v12, v13
.LBB0_613:
	s_or_b64 exec, exec, s[10:11]
	v_add_u32_e32 v13, 0x12700, v9
	v_mov_b32_e32 v16, v40
	v_mov_b32_e32 v17, v41
	v_mov_b32_e32 v18, v42
	v_mov_b32_e32 v19, v43
	v_add_u32_e32 v15, 0x15700, v9
	v_mov_b32_e32 v20, v44
	v_mov_b32_e32 v23, v45
	v_mov_b32_e32 v25, v46
	v_mov_b32_e32 v13, v48
	v_mov_b32_e32 v15, 3
	s_waitcnt lgkmcnt(5)
	v_mov_b32_e32 v22, v16
	s_waitcnt lgkmcnt(4)
	v_mov_b32_e32 v21, v19
	v_mov_b32_e32 v24, v17
	s_waitcnt lgkmcnt(0)
	v_mov_b32_e32 v19, v13
	v_pk_add_f32 v[20:21], v[20:21], v[22:23]
	v_pk_add_f32 v[16:17], v[24:25], v[18:19]
	s_nop 0
	v_pk_add_f32 v[16:17], v[20:21], v[16:17]
	s_nop 0
	v_add_f32_e32 v13, v16, v17
	v_cmp_ngt_f32_e64 s[8:9], v13, v14
	s_and_saveexec_b64 s[10:11], s[8:9]
	s_cbranch_execz .LBB0_617
	v_cmp_gt_f32_e64 s[8:9], v13, v12
	s_and_saveexec_b64 s[12:13], s[8:9]
	v_mov_b32_e32 v11, 3
	v_mov_b32_e32 v12, v13
	s_or_b64 exec, exec, s[12:13]
	v_mov_b32_e32 v15, v10
	v_mov_b32_e32 v10, v11
	v_mov_b32_e32 v13, v14
	v_mov_b32_e32 v14, v12
; DEVINL void phase4(const Params& P, unsigned char* smem) {
;     ...
;             const float g0 = LG(0), g1 = LG(1), g2 = LG(2), g3 = LG(3);
;             int gtop = 0; float gm = g0;
;             if (g1 > gm) { gm = g1; gtop = 1; } if (g2 > gm) { gm = g2; gtop = 2; } if (g3 > gm) { gm = g3; gtop = 3; }
;             const float gwt = 1.f / (expf(g0 - gm) + expf(g1 - gm) + expf(g2 - gm) + expf(g3 - gm));
;             int i1 = 0, i2 = 0; float v1 = -3.0e38f, v2 = -3.0e38f;
;             for (int e = 0; e < 8; ++e) {
;                 const float v = LG(4 + gtop * 8 + e);
;                 if (v > v1) { v2 = v1; i2 = i1; v1 = v; i1 = e; } else if (v > v2) { v2 = v; i2 = e; }
.LBB0_617:
	s_or_b64 exec, exec, s[10:11]
	v_add_u32_e32 v11, 0x12800, v9
	v_mov_b32_e32 v16, v50
	v_mov_b32_e32 v17, v51
	v_mov_b32_e32 v18, v52
	v_mov_b32_e32 v19, v53
	v_add_u32_e32 v12, 0x15800, v9
	v_mov_b32_e32 v20, v54
	v_mov_b32_e32 v23, v55
	v_mov_b32_e32 v25, v56
	v_mov_b32_e32 v11, v58
	s_waitcnt lgkmcnt(5)
	v_mov_b32_e32 v22, v16
	s_waitcnt lgkmcnt(4)
	v_mov_b32_e32 v21, v19
	v_mov_b32_e32 v24, v17
	s_waitcnt lgkmcnt(0)
	v_mov_b32_e32 v19, v11
	v_pk_add_f32 v[20:21], v[20:21], v[22:23]
	v_pk_add_f32 v[16:17], v[24:25], v[18:19]
	s_nop 0
	v_pk_add_f32 v[16:17], v[20:21], v[16:17]
	s_nop 0
	v_add_f32_e32 v12, v16, v17
	v_cmp_ngt_f32_e64 s[8:9], v12, v13
	v_mov_b32_e32 v16, 4
	s_and_saveexec_b64 s[10:11], s[8:9]
	s_cbranch_execz .LBB0_621
	v_cmp_gt_f32_e64 s[8:9], v12, v14
	s_and_saveexec_b64 s[12:13], s[8:9]
	v_mov_b32_e32 v10, 4
	v_mov_b32_e32 v14, v12
	s_or_b64 exec, exec, s[12:13]
	v_mov_b32_e32 v16, v15
	v_mov_b32_e32 v15, v10
	v_mov_b32_e32 v12, v13
	v_mov_b32_e32 v13, v14
.LBB0_621:
	s_or_b64 exec, exec, s[10:11]
	v_add_u32_e32 v14, 0x12900, v9
	v_mov_b32_e32 v10, v60
	v_mov_b32_e32 v11, v61
	v_mov_b32_e32 v18, v62
	v_mov_b32_e32 v19, v63
	v_add_u32_e32 v17, 0x15900, v9
	v_mov_b32_e32 v20, v64
	v_mov_b32_e32 v23, v65
	v_mov_b32_e32 v25, v66
	v_mov_b32_e32 v14, v68
	v_mov_b32_e32 v17, 5
	s_waitcnt lgkmcnt(5)
	v_mov_b32_e32 v22, v10
	s_waitcnt lgkmcnt(4)
	v_mov_b32_e32 v21, v19
	v_mov_b32_e32 v24, v11
	s_waitcnt lgkmcnt(0)
	v_mov_b32_e32 v19, v14
	v_pk_add_f32 v[20:21], v[20:21], v[22:23]
	v_pk_add_f32 v[10:11], v[24:25], v[18:19]
	s_nop 0
	v_pk_add_f32 v[10:11], v[20:21], v[10:11]
	s_nop 0
	v_add_f32_e32 v14, v10, v11
	v_cmp_ngt_f32_e64 s[8:9], v14, v12
	s_and_saveexec_b64 s[10:11], s[8:9]
	s_cbranch_execz .LBB0_625
	v_cmp_gt_f32_e64 s[8:9], v14, v13
	s_and_saveexec_b64 s[12:13], s[8:9]
	v_mov_b32_e32 v15, 5
	v_mov_b32_e32 v13, v14
	s_or_b64 exec, exec, s[12:13]
	v_mov_b32_e32 v17, v16
	v_mov_b32_e32 v16, v15
	v_mov_b32_e32 v14, v12
	v_mov_b32_e32 v12, v13
.LBB0_625:
	s_or_b64 exec, exec, s[10:11]
	v_add_u32_e32 v13, 0x12a00, v9
	v_mov_b32_e32 v10, v70
	v_mov_b32_e32 v11, v71
	v_mov_b32_e32 v18, v72
	v_mov_b32_e32 v19, v73
	v_add_u32_e32 v15, 0x15a00, v9
	v_mov_b32_e32 v20, v74
	v_mov_b32_e32 v23, v75
	v_mov_b32_e32 v25, v76
	v_mov_b32_e32 v13, v78
	s_waitcnt lgkmcnt(5)
	v_mov_b32_e32 v22, v10
	s_waitcnt lgkmcnt(4)
	v_mov_b32_e32 v21, v19
	v_mov_b32_e32 v24, v11
	s_waitcnt lgkmcnt(0)
	v_mov_b32_e32 v19, v13
	v_pk_add_f32 v[20:21], v[20:21], v[22:23]
	v_pk_add_f32 v[10:11], v[24:25], v[18:19]
	s_nop 0
	v_pk_add_f32 v[10:11], v[20:21], v[10:11]
	s_nop 0
	v_add_f32_e32 v11, v10, v11
	v_cmp_ngt_f32_e64 s[8:9], v11, v14
	v_mov_b32_e32 v10, 6
	s_and_saveexec_b64 s[10:11], s[8:9]
	s_cbranch_execz .LBB0_629
	v_cmp_gt_f32_e64 s[8:9], v11, v12
	s_and_saveexec_b64 s[12:13], s[8:9]
	v_mov_b32_e32 v16, 6
	v_mov_b32_e32 v12, v11
	s_or_b64 exec, exec, s[12:13]
	v_mov_b32_e32 v10, v17
	v_mov_b32_e32 v17, v16
	v_mov_b32_e32 v11, v14
	v_mov_b32_e32 v14, v12
.LBB0_629:
	s_or_b64 exec, exec, s[10:11]
	v_add_u32_e32 v15, 0x12b00, v9
	v_mov_b32_e32 v12, v80
	v_mov_b32_e32 v13, v81
	v_mov_b32_e32 v18, v82
	v_mov_b32_e32 v19, v83
	v_add_u32_e32 v16, 0x15b00, v9
	v_mov_b32_e32 v8, v84
	v_mov_b32_e32 v21, v85
	v_mov_b32_e32 v23, v86
	v_mov_b32_e32 v15, v88
	s_waitcnt lgkmcnt(5)
	v_mov_b32_e32 v20, v12
	s_waitcnt lgkmcnt(4)
	v_mov_b32_e32 v9, v19
	v_mov_b32_e32 v22, v13
	s_waitcnt lgkmcnt(0)
	v_mov_b32_e32 v19, v15
	v_pk_add_f32 v[8:9], v[8:9], v[20:21]
	v_pk_add_f32 v[12:13], v[22:23], v[18:19]
	s_nop 0
	v_pk_add_f32 v[8:9], v[8:9], v[12:13]
	s_nop 0
	v_add_f32_e32 v13, v8, v9
	v_cmp_ngt_f32_e64 s[8:9], v13, v11
	v_mov_b32_e32 v8, 7
	s_and_saveexec_b64 s[10:11], s[8:9]
	s_cbranch_execz .LBB0_633
	v_cmp_gt_f32_e64 s[8:9], v13, v14
	s_and_saveexec_b64 s[12:13], s[8:9]
	v_mov_b32_e32 v17, 7
	v_mov_b32_e32 v14, v13
	s_or_b64 exec, exec, s[12:13]
	v_mov_b32_e32 v8, v10
	v_mov_b32_e32 v10, v17
	v_mov_b32_e32 v13, v11
	v_mov_b32_e32 v11, v14

; DEVINL void phase5(const Params& P, unsigned char* smem) {
;     ...
;         for (int st = 64; st >= 1; st >>= 1) if (cls + st <= 111 && s_cp[cls + st] <= it) cls += st;
.LBB0_692:
	v_and_b32_e32 v2, 63, v0
	v_mov_b32_e32 v3, 0x24400
	v_lshl_add_u32 v2, v2, 2, v3
	ds_read_b32 v3, v2
	ds_read_b32 v4, v2 offset:256
	s_mov_b32 s30, -1
	s_mov_b32 s31, 0xffff
	s_waitcnt lgkmcnt(1)
	v_cmp_ge_i32_e32 vcc, s80, v3
	s_waitcnt lgkmcnt(0)
	v_cmp_ge_i32_e64 s[28:29], s80, v4
	s_bcnt1_i32_b64 s0, vcc
	s_and_b64 s[28:29], s[28:29], s[30:31]
	s_bcnt1_i32_b64 s1, s[28:29]
	s_add_i32 s0, s0, s1
	s_add_i32 s0, s0, -1

; DEVINL float bflo(unsigned u) { return __uint_as_float(u << 16); }
; DEVINL float bfhi(unsigned u) { return __uint_as_float(u & 0xffff0000u); }
; #define LDX1(mi_, buf_) { const int tk_ = s_tok[16 * (mi_) + lr2]; const bf16_t* xr_ = X1B + (size_t)(tk_ < 0 ? 0 : tk_) * DM + 128 * wv + 4 * g2; \
;                 _Pragma("unroll") for (int c_ = 0; c_ < 8; ++c_) xb[buf_][c_] = *(const u32x2*)(xr_ + 16 * c_); }
; DEVINL void phase5(const Params& P, unsigned char* smem) {
;     ...
;             for (int mi = 0; mi < 5; ++mi) {
;                 if (mi + 1 < 5) LDX1(mi + 1, (mi + 1) & 1)
;                 const int tok = s_tok[16 * mi + lr2];
;                 float qs = 0.f;
; #pragma unroll
;                 for (int w2 = 0; w2 < 8; ++w2) qs += s_part[w2 * 80 + 16 * mi + lr2];
;                 const float rstd = rsqrtf(qs * (1.f / DM) + EPS);
;                 const float* gfr = s_gfp + ((tok >> 13) & 1) * 1024 + 128 * wv + 4 * g2;
;                 float* orow = P.out + (size_t)(tok < 0 ? 0 : tok) * DM + 128 * wv + 4 * g2;
; #pragma unroll
;                 for (int c = 0; c < 8; ++c) {
;                     const f32x4 yv = c < 4 ? (f32x4){bflo(ypk[c & 3][mi].x), bfhi(ypk[c & 3][mi].x), bflo(ypk[c & 3][mi].y), bfhi(ypk[c & 3][mi].y)} : acc[c & 3][mi];
;                     const u32x2 xv = xb[mi & 1][c];
;                     const f32x4 x1 = {bflo(xv.x), bfhi(xv.x), bflo(xv.y), bfhi(xv.y)};
;                     const f32x4 gg = *(const f32x4*)(gfr + 16 * c);
;                     if (tok >= 0) *(f32x4*)(orow + 16 * c) = x1 + gg * (yv * rstd);
;                 }
.LBB0_738:
	s_or_b64 exec, exec, s[0:1]
	ds_read_b32 v194, v175 offset:256
	s_waitcnt lgkmcnt(0)
	v_cmp_lt_i32_e32 vcc, -1, v194
	s_and_saveexec_b64 s[0:1], vcc
	s_cbranch_execz .LBB0_691
	v_cvt_pk_bf16_f32 v35, v2, v3
	ds_read2_b32 v[2:3], v177 offset0:64 offset1:144
	v_cvt_pk_bf16_f32 v34, v4, v5
	ds_read2_b32 v[4:5], v156 offset0:96 offset1:176
	v_cvt_pk_bf16_f32 v39, v6, v7
	ds_read2_b32 v[6:7], v176 offset0:128 offset1:208
	s_waitcnt lgkmcnt(2)
	v_add_f32_e32 v2, 0, v2
	v_cvt_pk_bf16_f32 v38, v8, v9
	v_add_f32_e32 v8, v2, v3
	ds_read2_b32 v[2:3], v126 offset0:32 offset1:112
	s_waitcnt lgkmcnt(2)
	v_add_f32_e32 v4, v8, v4
	v_add_f32_e32 v4, v4, v5
	s_waitcnt lgkmcnt(1)
	v_add_f32_e32 v4, v4, v6
	v_add_f32_e32 v4, v4, v7
	s_waitcnt lgkmcnt(0)
	v_add_f32_e32 v2, v4, v2
	v_add_f32_e32 v2, v2, v3
	v_fmamk_f32 v2, v2, 0x3a800000, v221
	v_mul_f32_e32 v3, 0x4b800000, v2
	v_cmp_gt_f32_e32 vcc, s48, v2
	v_lshrrev_b32_e32 v4, 1, v194
	v_and_b32_e32 v4, 0x1000, v4
	v_cndmask_b32_e32 v2, v2, v3, vcc
	v_rsq_f32_e32 v2, v2
	v_cvt_pk_bf16_f32 v15, v14, v15
	v_add_u32_e32 v43, v174, v4
	v_lshlrev_b32_e32 v4, 16, v34
	v_mul_f32_e32 v3, 0x45800000, v2
	v_cndmask_b32_e32 v14, v2, v3, vcc
	v_and_b32_e32 v5, 0xffff0000, v34
	v_lshlrev_b32_e32 v6, 16, v35
	v_and_b32_e32 v7, 0xffff0000, v35
	v_cvt_pk_bf16_f32 v41, v24, v25
	v_pk_mul_f32 v[8:9], v[14:15], v[4:5] op_sel_hi:[0,1]
	v_pk_mul_f32 v[24:25], v[14:15], v[6:7] op_sel_hi:[0,1]
	ds_read_b128 v[4:7], v43
	v_cvt_pk_bf16_f32 v40, v20, v21
	v_cvt_pk_bf16_f32 v42, v22, v23
	v_lshlrev_b64 v[2:3], 12, v[194:195]
	ds_read_b128 v[20:23], v43 offset:64
	v_lshl_add_u64 v[2:3], s[12:13], 0, v[2:3]
	s_waitcnt vmcnt(7)
	v_and_b32_e32 v35, 0xffff0000, v75
	v_lshlrev_b32_e32 v36, 16, v74
	v_and_b32_e32 v37, 0xffff0000, v74
	v_lshlrev_b32_e32 v34, 16, v75
	v_lshl_add_u64 v[2:3], v[54:55], 2, v[2:3]
	s_waitcnt lgkmcnt(1)
	v_pk_fma_f32 v[6:7], v[6:7], v[24:25], v[34:35]
	v_pk_fma_f32 v[4:5], v[4:5], v[8:9], v[36:37]
	global_store_dwordx4 v[2:3], v[4:7], off
	s_waitcnt vmcnt(7)
	v_and_b32_e32 v9, 0xffff0000, v73
	v_lshlrev_b32_e32 v24, 16, v72
	v_lshlrev_b32_e32 v4, 16, v38
	v_and_b32_e32 v5, 0xffff0000, v38
	v_lshlrev_b32_e32 v6, 16, v39
	v_and_b32_e32 v7, 0xffff0000, v39
	v_pk_mul_f32 v[4:5], v[14:15], v[4:5] op_sel_hi:[0,1]
	v_pk_mul_f32 v[6:7], v[14:15], v[6:7] op_sel_hi:[0,1]
	v_and_b32_e32 v25, 0xffff0000, v72
	v_lshlrev_b32_e32 v8, 16, v73
	s_waitcnt lgkmcnt(0)
	v_pk_fma_f32 v[6:7], v[22:23], v[6:7], v[8:9]
	v_pk_fma_f32 v[4:5], v[20:21], v[4:5], v[24:25]
	global_store_dwordx4 v[2:3], v[4:7], off offset:64
	ds_read_b128 v[20:23], v43 offset:192
	s_waitcnt vmcnt(7)
	v_and_b32_e32 v35, 0xffff0000, v71
	v_lshlrev_b32_e32 v4, 16, v40
	v_and_b32_e32 v5, 0xffff0000, v40
	v_lshlrev_b32_e32 v6, 16, v15
	v_and_b32_e32 v7, 0xffff0000, v15
	v_pk_mul_f32 v[8:9], v[14:15], v[4:5] op_sel_hi:[0,1]
	v_pk_mul_f32 v[24:25], v[14:15], v[6:7] op_sel_hi:[0,1]
	ds_read_b128 v[4:7], v43 offset:128
	v_lshlrev_b32_e32 v36, 16, v70
	v_and_b32_e32 v37, 0xffff0000, v70
	v_lshlrev_b32_e32 v34, 16, v71
	v_pk_mul_f32 v[12:13], v[12:13], v[14:15] op_sel_hi:[1,0]
	s_waitcnt lgkmcnt(0)
	v_pk_fma_f32 v[6:7], v[6:7], v[24:25], v[34:35]
	v_pk_fma_f32 v[4:5], v[4:5], v[8:9], v[36:37]
	global_store_dwordx4 v[2:3], v[4:7], off offset:128
	s_waitcnt vmcnt(7)
	v_and_b32_e32 v9, 0xffff0000, v69
	v_lshlrev_b32_e32 v24, 16, v68
	v_lshlrev_b32_e32 v4, 16, v41
	v_and_b32_e32 v5, 0xffff0000, v41
	v_lshlrev_b32_e32 v6, 16, v42
	v_and_b32_e32 v7, 0xffff0000, v42
	v_pk_mul_f32 v[4:5], v[14:15], v[4:5] op_sel_hi:[0,1]
	v_pk_mul_f32 v[6:7], v[14:15], v[6:7] op_sel_hi:[0,1]
	v_and_b32_e32 v25, 0xffff0000, v68
	v_lshlrev_b32_e32 v8, 16, v69
	v_pk_fma_f32 v[6:7], v[22:23], v[6:7], v[8:9]
	v_pk_fma_f32 v[4:5], v[20:21], v[4:5], v[24:25]
	global_store_dwordx4 v[2:3], v[4:7], off offset:192
	ds_read_b128 v[4:7], v43 offset:256
	v_pk_mul_f32 v[20:21], v[10:11], v[14:15] op_sel_hi:[1,0]
	ds_read_b128 v[8:11], v43 offset:320
	s_waitcnt vmcnt(7)
	v_and_b32_e32 v23, 0xffff0000, v67
	v_lshlrev_b32_e32 v24, 16, v66
	v_and_b32_e32 v25, 0xffff0000, v66
	v_lshlrev_b32_e32 v22, 16, v67
	s_waitcnt lgkmcnt(1)
	v_pk_fma_f32 v[4:5], v[4:5], v[12:13], v[24:25]
	v_pk_fma_f32 v[6:7], v[6:7], v[20:21], v[22:23]
	global_store_dwordx4 v[2:3], v[4:7], off offset:256
	s_waitcnt vmcnt(7)
	v_and_b32_e32 v13, 0xffff0000, v65
	v_lshlrev_b32_e32 v12, 16, v65
	v_pk_mul_f32 v[6:7], v[16:17], v[14:15] op_sel_hi:[1,0]
	v_pk_mul_f32 v[4:5], v[18:19], v[14:15] op_sel_hi:[1,0]
	v_lshlrev_b32_e32 v16, 16, v64
	v_and_b32_e32 v17, 0xffff0000, v64
	s_waitcnt lgkmcnt(0)
	v_pk_fma_f32 v[4:5], v[4:5], v[8:9], v[16:17]
	v_pk_fma_f32 v[6:7], v[6:7], v[10:11], v[12:13]
	global_store_dwordx4 v[2:3], v[4:7], off offset:320
	ds_read_b128 v[4:7], v43 offset:384
	ds_read_b128 v[8:11], v43 offset:448
	v_pk_mul_f32 v[12:13], v[26:27], v[14:15] op_sel_hi:[1,0]
	v_pk_mul_f32 v[16:17], v[28:29], v[14:15] op_sel_hi:[1,0]
	s_waitcnt vmcnt(7)
	v_and_b32_e32 v19, 0xffff0000, v63
	v_lshlrev_b32_e32 v20, 16, v62
	v_and_b32_e32 v21, 0xffff0000, v62
	v_lshlrev_b32_e32 v18, 16, v63
	s_waitcnt lgkmcnt(1)
	v_pk_fma_f32 v[4:5], v[16:17], v[4:5], v[20:21]
	v_pk_fma_f32 v[6:7], v[12:13], v[6:7], v[18:19]
	global_store_dwordx4 v[2:3], v[4:7], off offset:384
	s_waitcnt vmcnt(7)
	v_and_b32_e32 v13, 0xffff0000, v57
	v_lshlrev_b32_e32 v12, 16, v57
	v_pk_mul_f32 v[6:7], v[30:31], v[14:15] op_sel_hi:[1,0]
	v_pk_mul_f32 v[4:5], v[32:33], v[14:15] op_sel_hi:[1,0]
	v_lshlrev_b32_e32 v14, 16, v56
	v_and_b32_e32 v15, 0xffff0000, v56
	s_waitcnt lgkmcnt(0)
	v_pk_fma_f32 v[4:5], v[4:5], v[8:9], v[14:15]
	v_pk_fma_f32 v[6:7], v[6:7], v[10:11], v[12:13]
	global_store_dwordx4 v[2:3], v[4:7], off offset:448
	s_branch .LBB0_691
.LBB0_744:
	s_endpgm
